# deferred weight-conversion split favouring gate/up tiles: 4096 + 1004 deferred, idle-slot quotas 6/9/8/10
# speedup vs baseline: 1.0030x; 1.0011x over previous
; __device__ __forceinline__ void bt_load(const float* __restrict__ src, int N, int perm, int it, int ntn, f32x4 (&v)[8]) {
;     const int wid = threadIdx.x >> 6, lane = threadIdx.x & 63;
;     const int per = 16 * ntn, z = it / per, r = it % per, kt = r / ntn, nt = r % ntn;
;     const int np = nt * 256 + lane * 4;
;     const int sc = perm ? (nt * 128 + (lane & 31) * 4 + (lane >> 5) * 1024) : np;
;     const float* p = src + (size_t)z * 1024 * N + (size_t)(kt * 64 + wid * 8) * N + sc;
; #pragma unroll
;     for (int i = 0; i < 8; ++i) v[i] = __builtin_nontemporal_load((const f32x4*)(p + (size_t)i * N));
; }
; __device__ __forceinline__ void ph_big_transpose(const float* __restrict__ src, int N, int perm, int batch, bf16* __restrict__ dst, float* tile  , int G, int ndefer) {
;     const int tid = threadIdx.x, wid = tid >> 6, lane = tid & 63, ntn = N / 256, total = batch * 16 * ntn - ndefer;
;     int it = (int)blockIdx.x;
;     if (it >= total) return;
;     f32x4 cur[8], nxt[8], nx2[8];
;     bt_load(src, N, perm, it, ntn, cur);
;     if (it + G < total) bt_load(src, N, perm, it + G, ntn, nxt);
.LBB0_71:
	s_cmpk_gt_i32 s2, 0xc13
	s_cbranch_scc1 .LBB0_79
	s_ashr_i32 s0, s2, 31
	s_lshr_b32 s0, s0, 26
	s_add_i32 s1, s2, s0
	s_ashr_i32 s0, s1, 6
	s_and_b32 s1, s1, 0xffc0
	s_sub_i32 s1, s2, s1
	s_bfe_i32 s4, s1, 0x80000
	s_bfe_u32 s4, s4, 0x2000d
	s_add_i32 s4, s1, s4
	s_bfe_i32 s5, s4, 0x80000
	s_and_b32 s4, s4, 0xfc
	s_sub_i32 s1, s1, s4
	v_lshlrev_b32_e32 v2, 2, v0
	s_sext_i32_i8 s1, s1
	v_and_b32_e32 v99, 0xfc, v2
	v_lshl_or_b32 v2, s1, 8, v99
	s_ashr_i32 s1, s0, 31
	s_lshl_b64 s[0:1], s[0:1], 22
	s_sext_i32_i16 s5, s5
	s_add_u32 s0, s72, s0
	s_addc_u32 s1, s73, s1
	s_lshl_b32 s4, s5, 4
	v_lshrrev_b32_e32 v3, 3, v0
	s_andn2_b32 s4, s4, 63
	v_and_b32_e32 v110, 56, v3
	v_or_b32_e32 v4, s4, v110
	v_ashrrev_i32_e32 v5, 31, v4
	v_lshlrev_b64 v[4:5], 12, v[4:5]
	v_lshl_add_u64 v[4:5], s[0:1], 0, v[4:5]
	v_ashrrev_i32_e32 v3, 31, v2
	v_lshl_add_u64 v[2:3], v[2:3], 2, v[4:5]
	s_movk_i32 s0, 0x2000
	v_add_co_u32_e32 v4, vcc, s0, v2
	s_movk_i32 s4, 0x4000
	s_nop 0
	v_addc_co_u32_e32 v5, vcc, 0, v3, vcc
	global_load_dwordx4 v[42:45], v[4:5], off offset:-4096 nt
	global_load_dwordx4 v[34:37], v[4:5], off nt
	v_add_co_u32_e32 v4, vcc, s4, v2
	s_movk_i32 s1, 0x5000
	s_nop 0
	v_addc_co_u32_e32 v5, vcc, 0, v3, vcc
	global_load_dwordx4 v[46:49], v[4:5], off offset:-4096 nt
	global_load_dwordx4 v[38:41], v[4:5], off nt
	v_add_co_u32_e32 v4, vcc, s1, v2
	s_add_i32 s5, s62, s2
	s_nop 0
	v_addc_co_u32_e32 v5, vcc, 0, v3, vcc
	global_load_dwordx4 v[62:65], v[2:3], off nt
	global_load_dwordx4 v[50:53], v[4:5], off nt
	v_add_co_u32_e32 v4, vcc, 0x6000, v2
	s_cmpk_gt_i32 s5, 0xc13
	s_nop 0
	v_addc_co_u32_e32 v5, vcc, 0, v3, vcc
	v_add_co_u32_e32 v2, vcc, 0x7000, v2
	s_movk_i32 s1, 0x3000
	s_nop 0
	v_addc_co_u32_e32 v3, vcc, 0, v3, vcc
	global_load_dwordx4 v[58:61], v[4:5], off nt
	global_load_dwordx4 v[54:57], v[2:3], off nt
	s_cbranch_scc1 .LBB0_74
	s_ashr_i32 s6, s5, 31
	s_lshr_b32 s6, s6, 26
	s_add_i32 s7, s5, s6
	s_ashr_i32 s6, s7, 6
	s_and_b32 s7, s7, 0xffc0
	s_sub_i32 s5, s5, s7
	s_bfe_i32 s7, s5, 0x80000
	s_bfe_u32 s7, s7, 0x2000d
	s_add_i32 s7, s5, s7
	s_bfe_i32 s8, s7, 0x80000
	s_and_b32 s7, s7, 0xfc
	s_sub_i32 s5, s5, s7
	s_ashr_i32 s7, s6, 31
	s_lshl_b64 s[6:7], s[6:7], 22
	s_sext_i32_i16 s8, s8
	s_sext_i32_i8 s5, s5
	s_add_u32 s6, s72, s6
	v_lshl_or_b32 v2, s5, 8, v99
	s_addc_u32 s7, s73, s7
	s_lshl_b32 s5, s8, 4
	s_andn2_b32 s5, s5, 63
	v_or_b32_e32 v4, s5, v110
	v_ashrrev_i32_e32 v5, 31, v4
	v_lshlrev_b64 v[4:5], 12, v[4:5]
	v_lshl_add_u64 v[4:5], s[6:7], 0, v[4:5]
	v_ashrrev_i32_e32 v3, 31, v2
	v_lshl_add_u64 v[26:27], v[2:3], 2, v[4:5]
	v_add_co_u32_e32 v2, vcc, s0, v26
	s_nop 1
	v_addc_co_u32_e32 v3, vcc, 0, v27, vcc
	v_add_co_u32_e32 v10, vcc, s4, v26
	global_load_dwordx4 v[6:9], v[2:3], off offset:-4096 nt
	s_nop 0
	global_load_dwordx4 v[2:5], v[2:3], off nt
	v_addc_co_u32_e32 v11, vcc, 0, v27, vcc
	v_add_co_u32_e32 v18, vcc, 0x5000, v26
	global_load_dwordx4 v[14:17], v[10:11], off offset:-4096 nt
	s_nop 0
	global_load_dwordx4 v[10:13], v[10:11], off nt
	v_addc_co_u32_e32 v19, vcc, 0, v27, vcc
	v_add_co_u32_e32 v28, vcc, 0x6000, v26
	global_load_dwordx4 v[22:25], v[26:27], off nt
	s_nop 0
	global_load_dwordx4 v[18:21], v[18:19], off nt
	v_addc_co_u32_e32 v29, vcc, 0, v27, vcc
	v_add_co_u32_e32 v30, vcc, 0x7000, v26
	s_nop 1
	v_addc_co_u32_e32 v31, vcc, 0, v27, vcc
	global_load_dwordx4 v[26:29], v[28:29], off nt
	s_nop 0
	global_load_dwordx4 v[30:33], v[30:31], off nt

; __device__ __forceinline__ void bt_load(const float* __restrict__ src, int N, int perm, int it, int ntn, f32x4 (&v)[8]) {
;     const int wid = threadIdx.x >> 6, lane = threadIdx.x & 63;
;     const int per = 16 * ntn, z = it / per, r = it % per, kt = r / ntn, nt = r % ntn;
;     const int np = nt * 256 + lane * 4;
;     const int sc = perm ? (nt * 128 + (lane & 31) * 4 + (lane >> 5) * 1024) : np;
;     const float* p = src + (size_t)z * 1024 * N + (size_t)(kt * 64 + wid * 8) * N + sc;
; #pragma unroll
;     for (int i = 0; i < 8; ++i) v[i] = __builtin_nontemporal_load((const f32x4*)(p + (size_t)i * N));
; }
; __device__ __forceinline__ void ph_big_transpose(const float* __restrict__ src, int N, int perm, int batch, bf16* __restrict__ dst, float* tile  , int G, int ndefer) {
;     const int tid = threadIdx.x, wid = tid >> 6, lane = tid & 63, ntn = N / 256, total = batch * 16 * ntn - ndefer;
;     int it = (int)blockIdx.x;
;     if (it >= total) return;
;     f32x4 cur[8], nxt[8], nx2[8];
;     bt_load(src, N, perm, it, ntn, cur);
;     if (it + G < total) bt_load(src, N, perm, it + G, ntn, nxt);
;     for (; it < total; it += G) {
;         const bool more = it + G < total, more2 = it + 2 * G < total;
;         if (more2) bt_load(src, N, perm, it + 2 * G, ntn, nx2);
;         __syncthreads();
; #pragma unroll
;         for (int i = 0; i < 8; ++i) { float* t = tile + (wid * 8 + i) * 257 + lane * 4; t[0] = cur[i][0]; t[1] = cur[i][1]; t[2] = cur[i][2]; t[3] = cur[i][3]; }
;         __syncthreads();
;         const int per = 16 * ntn, z = it / per, r = it % per, kt = r / ntn, nt = r % ntn;
;         bf16* d = dst + (size_t)z * N * 1024 + (((size_t)nt * 16 + kt) << 14);
;         const int kc = lane & 7;
; #pragma unroll
;         for (int pss = 0; pss < 4; ++pss) {
;             const int n = wid * 32 + pss * 8 + (lane >> 3); float f[8];
; #pragma unroll
;             for (int j = 0; j < 8; ++j) f[j] = tile[(kc * 8 + j) * 257 + n];
;             u32x4 w; w.x = g8_cvt_pk(f[0], f[1]); w.y = g8_cvt_pk(f[2], f[3]); w.z = g8_cvt_pk(f[4], f[5]); w.w = g8_cvt_pk(f[6], f[7]);
;             __builtin_nontemporal_store(w, (u32x4*)(d + n * 64 + kc * 8));
;         }
;         if (more) {
; #pragma unroll
;             for (int i = 0; i < 8; ++i) { cur[i] = nxt[i]; nxt[i] = nx2[i]; } }
;     }
.LBB0_75:
	s_ashr_i32 s8, s3, 31
	s_barrier
	s_waitcnt vmcnt(3)
	ds_write_b128 v111, v[62:65]
	v_add_u32_e32 v62, 0x404, v111
	s_lshr_b32 s8, s8, 26
	ds_write2_b32 v62, v42, v43 offset1:1
	v_add_u32_e32 v42, 0x40c, v111
	s_add_i32 s9, s3, s8
	ds_write2_b32 v42, v44, v45 offset1:1
	v_add_u32_e32 v42, 0x808, v111
	s_ashr_i32 s8, s9, 6
	s_and_b32 s9, s9, 0xffc0
	s_add_i32 s7, s3, s62
	ds_write2_b64 v42, v[34:35], v[36:37] offset1:1
	v_add_u32_e32 v34, 0xc0c, v111
	s_sub_i32 s3, s3, s9
	ds_write2_b32 v34, v46, v47 offset1:1
	v_add_u32_e32 v34, 0xc14, v111
	s_bfe_i32 s9, s3, 0x80000
	ds_write2_b32 v34, v48, v49 offset1:1
	ds_write_b128 v111, v[38:41] offset:4112
	v_add_u32_e32 v34, 0x1414, v111
	s_bfe_u32 s9, s9, 0x2000d
	s_waitcnt vmcnt(2)
	ds_write2_b32 v34, v50, v51 offset1:1
	v_add_u32_e32 v34, 0x141c, v111
	s_add_i32 s9, s3, s9
	ds_write2_b32 v34, v52, v53 offset1:1
	v_add_u32_e32 v34, 0x1818, v111
	s_bfe_i32 s10, s9, 0x80000
	s_and_b32 s9, s9, 0xfc
	s_waitcnt vmcnt(1)
	ds_write2_b64 v34, v[58:59], v[60:61] offset1:1
	v_add_u32_e32 v34, 0x1c1c, v111
	s_sext_i32_i16 s10, s10
	s_sub_i32 s30, s3, s9
	s_ashr_i32 s9, s8, 31
	s_waitcnt vmcnt(0)
	ds_write2_b32 v34, v54, v55 offset1:1
	v_add_u32_e32 v34, 0x1c24, v111
	s_lshr_b32 s10, s10, 2
	s_lshl_b64 s[8:9], s[8:9], 21
	ds_write2_b32 v34, v56, v57 offset1:1
	s_waitcnt lgkmcnt(0)
	s_barrier
	s_add_u32 s3, s4, s8
	ds_read_b32 v34, v112 offset:1028
	ds_read_b32 v35, v112 offset:3084
	ds_read_b32 v36, v112 offset:5140
	ds_read_b32 v37, v112 offset:7196
	ds_read_b32 v38, v112 offset:6168
	ds_read_b32 v39, v112 offset:4112
	ds_read_b32 v40, v112 offset:2056
	ds_read_b32 v41, v112
	s_addc_u32 s31, s5, s9
	s_bfe_i64 s[8:9], s[30:31], 0x80000
	s_bfe_i64 s[10:11], s[10:11], 0x100000
	s_lshl_b64 s[8:9], s[8:9], 19
	s_add_u32 s3, s3, s8
	s_addc_u32 s30, s31, s9
	s_lshl_b64 s[8:9], s[10:11], 15
	s_waitcnt lgkmcnt(0)
	v_cvt_pk_bf16_f32 v34, v41, v34
	v_cvt_pk_bf16_f32 v35, v40, v35
	v_cvt_pk_bf16_f32 v36, v39, v36
	v_cvt_pk_bf16_f32 v37, v38, v37
	ds_read_b32 v42, v112 offset:1060
	ds_read_b32 v43, v112 offset:3116
	ds_read_b32 v44, v112 offset:5172
	ds_read_b32 v45, v112 offset:7228
	ds_read_b32 v46, v112 offset:6200
	ds_read_b32 v47, v112 offset:4144
	ds_read_b32 v48, v112 offset:2088
	ds_read_b32 v49, v112 offset:32
	s_add_u32 s8, s3, s8
	s_addc_u32 s9, s30, s9
	v_lshl_add_u64 v[38:39], s[8:9], 0, v[100:101]
	v_mov_b32_e32 v103, v101
	v_lshl_add_u64 v[40:41], v[38:39], 0, v[102:103]
	global_store_dwordx4 v[40:41], v[34:37], off nt
	v_mov_b32_e32 v105, v101
	v_lshl_add_u64 v[40:41], v[38:39], 0, v[104:105]
	s_waitcnt lgkmcnt(0)
	v_cvt_pk_bf16_f32 v34, v49, v42
	v_cvt_pk_bf16_f32 v35, v48, v43
	v_cvt_pk_bf16_f32 v36, v47, v44
	v_cvt_pk_bf16_f32 v37, v46, v45
	ds_read_b32 v42, v112 offset:1092
	ds_read_b32 v43, v112 offset:3148
	ds_read_b32 v44, v112 offset:5204
	ds_read_b32 v45, v112 offset:6232
	ds_read_b32 v46, v112 offset:4176
	ds_read_b32 v47, v112 offset:2120
	ds_read_b32 v48, v112 offset:64
	ds_read_b32 v49, v112 offset:7260
	global_store_dwordx4 v[40:41], v[34:37], off nt
	v_mov_b32_e32 v107, v101
	v_lshl_add_u64 v[40:41], v[38:39], 0, v[106:107]
	s_waitcnt lgkmcnt(1)
	v_cvt_pk_bf16_f32 v34, v48, v42
	v_cvt_pk_bf16_f32 v35, v47, v43
	v_cvt_pk_bf16_f32 v36, v46, v44
	s_waitcnt lgkmcnt(0)
	v_cvt_pk_bf16_f32 v37, v45, v49
	ds_read_b32 v42, v112 offset:1124
	ds_read_b32 v43, v112 offset:3180
	ds_read_b32 v44, v112 offset:5236
	ds_read_b32 v45, v112 offset:6264
	ds_read_b32 v46, v112 offset:4208
	ds_read_b32 v47, v112 offset:2152
	ds_read_b32 v48, v112 offset:96
	ds_read_b32 v49, v112 offset:7292
	v_mov_b32_e32 v109, v101
	global_store_dwordx4 v[40:41], v[34:37], off nt
	v_lshl_add_u64 v[38:39], v[38:39], 0, v[108:109]
	v_mov_b64_e32 v[56:57], v[32:33]
	s_waitcnt lgkmcnt(1)
	v_cvt_pk_bf16_f32 v34, v48, v42
	v_cvt_pk_bf16_f32 v35, v47, v43
	v_cvt_pk_bf16_f32 v36, v46, v44
	s_waitcnt lgkmcnt(0)
	v_cvt_pk_bf16_f32 v37, v45, v49
	global_store_dwordx4 v[38:39], v[34:37], off nt
	v_mov_b64_e32 v[60:61], v[28:29]
	v_mov_b64_e32 v[52:53], v[20:21]
	v_mov_b64_e32 v[40:41], v[12:13]
	v_mov_b64_e32 v[48:49], v[16:17]
	v_mov_b64_e32 v[36:37], v[4:5]
	v_mov_b64_e32 v[44:45], v[8:9]
	v_mov_b64_e32 v[64:65], v[24:25]
	v_mov_b64_e32 v[54:55], v[30:31]
	v_mov_b64_e32 v[58:59], v[26:27]
	v_mov_b64_e32 v[50:51], v[18:19]
	v_mov_b64_e32 v[38:39], v[10:11]
	v_mov_b64_e32 v[46:47], v[14:15]
	v_mov_b64_e32 v[34:35], v[2:3]
	v_mov_b64_e32 v[42:43], v[6:7]
	v_mov_b64_e32 v[62:63], v[22:23]
	v_mov_b64_e32 v[30:31], v[94:95]
	v_mov_b64_e32 v[26:27], v[90:91]
	v_mov_b64_e32 v[18:19], v[86:87]
	v_mov_b64_e32 v[10:11], v[82:83]
	v_mov_b64_e32 v[14:15], v[74:75]
	v_mov_b64_e32 v[2:3], v[66:67]
	v_mov_b64_e32 v[6:7], v[70:71]
	v_mov_b64_e32 v[22:23], v[78:79]
	s_cmpk_lt_i32 s7, 0xc14
	v_mov_b64_e32 v[32:33], v[96:97]
	v_mov_b64_e32 v[28:29], v[92:93]
	v_mov_b64_e32 v[20:21], v[88:89]
	v_mov_b64_e32 v[12:13], v[84:85]
	v_mov_b64_e32 v[16:17], v[76:77]
	v_mov_b64_e32 v[4:5], v[68:69]
	v_mov_b64_e32 v[8:9], v[72:73]
	v_mov_b64_e32 v[24:25], v[80:81]
	s_mov_b32 s3, s7
	s_cbranch_scc0 .LBB0_78
.LBB0_76:
	s_add_i32 s7, s6, s3
	s_cmpk_gt_i32 s7, 0xc13
	s_cbranch_scc1 .LBB0_75
	s_ashr_i32 s8, s7, 31
	s_lshr_b32 s8, s8, 26
	s_add_i32 s9, s7, s8
	s_ashr_i32 s8, s9, 6
	s_and_b32 s9, s9, 0xffc0
	s_sub_i32 s7, s7, s9
	s_bfe_i32 s9, s7, 0x80000
	s_bfe_u32 s9, s9, 0x2000d
	s_add_i32 s9, s7, s9
	s_bfe_i32 s10, s9, 0x80000
	s_and_b32 s9, s9, 0xfc
	s_sub_i32 s7, s7, s9
	s_ashr_i32 s9, s8, 31
	s_lshl_b64 s[8:9], s[8:9], 22
	s_sext_i32_i16 s10, s10
	s_sext_i32_i8 s7, s7
	s_add_u32 s8, s72, s8
	v_lshl_or_b32 v66, s7, 8, v99
	s_addc_u32 s9, s73, s9
	s_lshl_b32 s7, s10, 4
	s_andn2_b32 s7, s7, 63
	v_or_b32_e32 v68, s7, v110
	v_ashrrev_i32_e32 v69, 31, v68
	v_lshlrev_b64 v[68:69], 12, v[68:69]
	v_lshl_add_u64 v[68:69], s[8:9], 0, v[68:69]
	v_ashrrev_i32_e32 v67, 31, v66
	v_lshl_add_u64 v[90:91], v[66:67], 2, v[68:69]
	v_add_co_u32_e32 v66, vcc, s0, v90
	s_nop 1
	v_addc_co_u32_e32 v67, vcc, 0, v91, vcc
	v_add_co_u32_e32 v74, vcc, s1, v90
	global_load_dwordx4 v[70:73], v[66:67], off offset:-4096 nt
	s_nop 0
	global_load_dwordx4 v[66:69], v[66:67], off nt
	v_addc_co_u32_e32 v75, vcc, 0, v91, vcc
	v_add_co_u32_e32 v82, vcc, 0x4000, v90
	global_load_dwordx4 v[78:81], v[90:91], off nt
	s_nop 0
	global_load_dwordx4 v[74:77], v[74:75], off nt
	v_addc_co_u32_e32 v83, vcc, 0, v91, vcc
	v_add_co_u32_e32 v86, vcc, 0x5000, v90
	s_nop 1
	v_addc_co_u32_e32 v87, vcc, 0, v91, vcc
	v_add_co_u32_e32 v92, vcc, 0x6000, v90
	global_load_dwordx4 v[82:85], v[82:83], off nt
	s_nop 0
	global_load_dwordx4 v[86:89], v[86:87], off nt
	v_addc_co_u32_e32 v93, vcc, 0, v91, vcc
	v_add_co_u32_e32 v94, vcc, 0x7000, v90
	s_nop 1
	v_addc_co_u32_e32 v95, vcc, 0, v91, vcc
	global_load_dwordx4 v[90:93], v[92:93], off nt
	s_nop 0
	global_load_dwordx4 v[94:97], v[94:95], off nt
	s_branch .LBB0_75
